# attention loop with one LDS wait per four fragments (lookahead 8)
# baseline (speedup 1.0000x reference)
.Lattn_pa0:
	s_waitcnt lgkmcnt(4)
	v_mfma_f32_16x16x32_bf16 v[64:67], v[160:163], v[96:99], 0
	v_exp_f32_e32 v88, v88
	v_mfma_f32_16x16x32_bf16 v[68:71], v[160:163], v[112:115], 0
	v_exp_f32_e32 v92, v92
	ds_read_b128 v[160:163], v201 offset:20480
	s_add_u32 s16, s22, s10
	s_addc_u32 s17, s23, s11
	s_add_u32 s15, s22, s12
	s_addc_u32 s14, s23, s13
	s_add_u32 s8, s16, 0x3bc00200
	s_addc_u32 s9, s17, 0
	s_add_u32 s6, s15, 0x23a50000
	s_addc_u32 s7, s14, 0
	v_mfma_f32_16x16x32_bf16 v[0:3], v[164:167], v[216:219], v[0:3]
	v_cvt_pk_bf16_f32 v242, v80, v81
	v_mfma_f32_16x16x32_bf16 v[4:7], v[164:167], v[238:241], v[4:7]
	v_exp_f32_e32 v89, v89
	ds_read_b128 v[164:167], v209 offset:8192
	s_waitcnt vmcnt(4)
	ds_write_b128 v225, v[152:155] offset:49152
	v_mfma_f32_16x16x32_bf16 v[68:71], v[168:171], v[116:119], v[68:71]
	v_exp_f32_e32 v93, v93
	v_mfma_f32_16x16x32_bf16 v[64:67], v[168:171], v[100:103], v[64:67]
	v_cvt_pk_bf16_f32 v243, v82, v83
	ds_read_b128 v[168:171], v202 offset:20480
	ds_write_b128 v226, v[156:159] offset:49152
	v_mfma_f32_16x16x32_bf16 v[12:15], v[172:175], v[238:241], v[12:15]
	v_exp_f32_e32 v90, v90
	v_mfma_f32_16x16x32_bf16 v[8:11], v[172:175], v[216:219], v[8:11]
	v_exp_f32_e32 v94, v94
	ds_read_b128 v[172:175], v209 offset:10240
	ds_write_b64 v227, v[132:133] offset:32768
	s_waitcnt lgkmcnt(7)
	v_mfma_f32_16x16x32_bf16 v[64:67], v[176:179], v[104:107], v[64:67]
	v_cvt_pk_bf16_f32 v204, v84, v85
	v_mfma_f32_16x16x32_bf16 v[68:71], v[176:179], v[120:123], v[68:71]
	v_exp_f32_e32 v91, v91
	ds_read_b128 v[176:179], v203 offset:20480
	ds_write_b64 v228, v[134:135] offset:32768
	v_mfma_f32_16x16x32_bf16 v[16:19], v[180:183], v[216:219], v[16:19]
	v_exp_f32_e32 v95, v95
	v_mfma_f32_16x16x32_bf16 v[20:23], v[180:183], v[238:241], v[20:23]
	v_cvt_pk_bf16_f32 v205, v86, v87
	v_add_f32_e32 v220, v220, v88
	ds_read_b128 v[180:183], v209 offset:12288
	ds_write_b64 v229, v[128:129] offset:32768
	v_mfma_f32_16x16x32_bf16 v[68:71], v[230:233], v[124:127], v[68:71]
	v_add_f32_e32 v221, v221, v92
	v_add_f32_e32 v220, v220, v89
	v_mfma_f32_16x16x32_bf16 v[64:67], v[230:233], v[108:111], v[64:67]
	v_add_f32_e32 v221, v221, v93
	v_cvt_pk_bf16_f32 v244, v88, v89
	ds_read_b128 v[230:233], v246 offset:20480
	ds_write_b64 v184, v[130:131] offset:32768
	v_mfma_f32_16x16x32_bf16 v[28:31], v[234:237], v[238:241], v[28:31]
	v_cvt_pk_bf16_f32 v245, v90, v91
	v_cvt_pk_bf16_f32 v206, v92, v93
	v_mfma_f32_16x16x32_bf16 v[24:27], v[234:237], v[216:219], v[24:27]
	v_cvt_pk_bf16_f32 v207, v94, v95
	ds_read_b128 v[234:237], v209 offset:14336
	global_load_dwordx4 v[132:135], v198, s[8:9]
	s_waitcnt lgkmcnt(8)
	v_mfma_f32_16x16x32_bf16 v[72:75], v[160:163], v[96:99], 0
	v_add_f32_e32 v220, v220, v90
	v_add_f32_e32 v221, v221, v94
	v_mfma_f32_16x16x32_bf16 v[76:79], v[160:163], v[112:115], 0
	v_add_f32_e32 v220, v220, v91
	v_add_f32_e32 v221, v221, v95
	ds_read_b128 v[160:163], v201 offset:24576
	global_load_dwordx4 v[128:131], v199, s[8:9]
	v_mfma_f32_16x16x32_bf16 v[32:35], v[164:167], v[216:219], v[32:35]
	v_add_f32_e32 v194, v194, v220
	v_add_f32_e32 v195, v195, v221
	v_mfma_f32_16x16x32_bf16 v[36:39], v[164:167], v[238:241], v[36:39]
	v_exp_f32_e32 v64, v64
	ds_read_b128 v[164:167], v210 offset:0
	global_load_dwordx4 v[152:155], v196, s[6:7]
	v_mfma_f32_16x16x32_bf16 v[76:79], v[168:171], v[116:119], v[76:79]
	v_exp_f32_e32 v68, v68
	v_mfma_f32_16x16x32_bf16 v[72:75], v[168:171], v[100:103], v[72:75]
	v_exp_f32_e32 v65, v65
	ds_read_b128 v[168:171], v202 offset:24576
	global_load_dwordx4 v[156:159], v197, s[6:7]
	v_mfma_f32_16x16x32_bf16 v[44:47], v[172:175], v[238:241], v[44:47]
	v_exp_f32_e32 v69, v69
	v_mfma_f32_16x16x32_bf16 v[40:43], v[172:175], v[216:219], v[40:43]
	v_exp_f32_e32 v66, v66
	ds_read_b128 v[172:175], v210 offset:2048
	s_waitcnt lgkmcnt(4)
	v_mfma_f32_16x16x32_bf16 v[72:75], v[176:179], v[104:107], v[72:75]
	v_exp_f32_e32 v70, v70
	v_mfma_f32_16x16x32_bf16 v[76:79], v[176:179], v[120:123], v[76:79]
	v_exp_f32_e32 v67, v67
	ds_read_b128 v[176:179], v203 offset:24576
	v_mfma_f32_16x16x32_bf16 v[48:51], v[180:183], v[216:219], v[48:51]
	v_exp_f32_e32 v71, v71
	v_mfma_f32_16x16x32_bf16 v[52:55], v[180:183], v[238:241], v[52:55]
	v_add_f32_e32 v220, v64, v65
	ds_read_b128 v[180:183], v210 offset:4096
	v_mfma_f32_16x16x32_bf16 v[76:79], v[230:233], v[124:127], v[76:79]
	v_add_f32_e32 v221, v68, v69
	v_mfma_f32_16x16x32_bf16 v[72:75], v[230:233], v[108:111], v[72:75]
	v_add_f32_e32 v220, v220, v66
	ds_read_b128 v[230:233], v246 offset:24576
	v_mfma_f32_16x16x32_bf16 v[60:63], v[234:237], v[238:241], v[60:63]
	v_add_f32_e32 v221, v221, v70
	v_add_f32_e32 v220, v220, v67
	v_mfma_f32_16x16x32_bf16 v[56:59], v[234:237], v[216:219], v[56:59]
	v_add_f32_e32 v221, v221, v71
	ds_read_b128 v[234:237], v210 offset:6144
	s_waitcnt lgkmcnt(4)
	v_mfma_f32_16x16x32_bf16 v[80:83], v[160:163], v[96:99], 0
	v_exp_f32_e32 v72, v72
	v_mfma_f32_16x16x32_bf16 v[84:87], v[160:163], v[112:115], 0
	v_exp_f32_e32 v76, v76
	ds_read_b128 v[160:163], v201 offset:28672
	v_mfma_f32_16x16x32_bf16 v[0:3], v[164:167], v[242:245], v[0:3]
	v_exp_f32_e32 v73, v73
	v_mfma_f32_16x16x32_bf16 v[4:7], v[164:167], v[204:207], v[4:7]
	v_exp_f32_e32 v77, v77
	ds_read_b128 v[164:167], v210 offset:8192
	v_mfma_f32_16x16x32_bf16 v[84:87], v[168:171], v[116:119], v[84:87]
	v_exp_f32_e32 v74, v74
	v_mfma_f32_16x16x32_bf16 v[80:83], v[168:171], v[100:103], v[80:83]
	v_exp_f32_e32 v78, v78
	ds_read_b128 v[168:171], v202 offset:28672
	v_mfma_f32_16x16x32_bf16 v[12:15], v[172:175], v[204:207], v[12:15]
	v_exp_f32_e32 v75, v75
	v_mfma_f32_16x16x32_bf16 v[8:11], v[172:175], v[242:245], v[8:11]
	v_exp_f32_e32 v79, v79
	ds_read_b128 v[172:175], v210 offset:10240
	s_waitcnt lgkmcnt(4)
	v_mfma_f32_16x16x32_bf16 v[80:83], v[176:179], v[104:107], v[80:83]
	v_add_f32_e32 v220, v220, v72
	v_add_f32_e32 v221, v221, v76
	v_mfma_f32_16x16x32_bf16 v[84:87], v[176:179], v[120:123], v[84:87]
	v_add_f32_e32 v220, v220, v73
	ds_read_b128 v[176:179], v203 offset:28672
	v_mfma_f32_16x16x32_bf16 v[16:19], v[180:183], v[242:245], v[16:19]
	v_add_f32_e32 v221, v221, v77
	v_add_f32_e32 v220, v220, v74
	v_mfma_f32_16x16x32_bf16 v[20:23], v[180:183], v[204:207], v[20:23]
	v_add_f32_e32 v221, v221, v78
	ds_read_b128 v[180:183], v210 offset:12288
	v_mfma_f32_16x16x32_bf16 v[84:87], v[230:233], v[124:127], v[84:87]
	v_add_f32_e32 v220, v220, v75
	v_add_f32_e32 v221, v221, v79
	v_mfma_f32_16x16x32_bf16 v[80:83], v[230:233], v[108:111], v[80:83]
	v_cvt_pk_bf16_f32 v216, v64, v65
	ds_read_b128 v[230:233], v246 offset:28672
	v_mfma_f32_16x16x32_bf16 v[28:31], v[234:237], v[204:207], v[28:31]
	v_cvt_pk_bf16_f32 v217, v66, v67
	v_cvt_pk_bf16_f32 v238, v68, v69
	v_mfma_f32_16x16x32_bf16 v[24:27], v[234:237], v[242:245], v[24:27]
	v_cvt_pk_bf16_f32 v239, v70, v71
	ds_read_b128 v[234:237], v210 offset:14336
	s_waitcnt lgkmcnt(4)
	v_mfma_f32_16x16x32_bf16 v[88:91], v[160:163], v[96:99], 0
	v_exp_f32_e32 v80, v80
	v_mfma_f32_16x16x32_bf16 v[92:95], v[160:163], v[112:115], 0
	v_exp_f32_e32 v84, v84
	ds_read_b128 v[160:163], v201 offset:32768
	v_mfma_f32_16x16x32_bf16 v[32:35], v[164:167], v[242:245], v[32:35]
	v_exp_f32_e32 v81, v81
	v_mfma_f32_16x16x32_bf16 v[36:39], v[164:167], v[204:207], v[36:39]
	v_exp_f32_e32 v85, v85
	ds_read_b128 v[164:167], v209 offset:16384
	v_mfma_f32_16x16x32_bf16 v[92:95], v[168:171], v[116:119], v[92:95]
	v_exp_f32_e32 v82, v82
	v_mfma_f32_16x16x32_bf16 v[88:91], v[168:171], v[100:103], v[88:91]
	v_exp_f32_e32 v86, v86
	ds_read_b128 v[168:171], v202 offset:32768
	v_mfma_f32_16x16x32_bf16 v[44:47], v[172:175], v[204:207], v[44:47]
	v_exp_f32_e32 v83, v83
	v_mfma_f32_16x16x32_bf16 v[40:43], v[172:175], v[242:245], v[40:43]
	v_exp_f32_e32 v87, v87
	ds_read_b128 v[172:175], v209 offset:18432
	s_waitcnt lgkmcnt(4)
	v_mfma_f32_16x16x32_bf16 v[88:91], v[176:179], v[104:107], v[88:91]
	v_add_f32_e32 v220, v220, v80
	v_add_f32_e32 v221, v221, v84
	v_mfma_f32_16x16x32_bf16 v[92:95], v[176:179], v[120:123], v[92:95]
	v_add_f32_e32 v220, v220, v81
	ds_read_b128 v[176:179], v203 offset:32768
	v_mfma_f32_16x16x32_bf16 v[48:51], v[180:183], v[242:245], v[48:51]
	v_add_f32_e32 v221, v221, v85
	v_add_f32_e32 v220, v220, v82
	v_mfma_f32_16x16x32_bf16 v[52:55], v[180:183], v[204:207], v[52:55]
	v_add_f32_e32 v221, v221, v86
	ds_read_b128 v[180:183], v209 offset:20480
	v_mfma_f32_16x16x32_bf16 v[92:95], v[230:233], v[124:127], v[92:95]
	v_add_f32_e32 v220, v220, v83
	v_add_f32_e32 v221, v221, v87
	v_mfma_f32_16x16x32_bf16 v[88:91], v[230:233], v[108:111], v[88:91]
	v_cvt_pk_bf16_f32 v218, v72, v73
	ds_read_b128 v[230:233], v246 offset:32768
	v_mfma_f32_16x16x32_bf16 v[60:63], v[234:237], v[204:207], v[60:63]
	v_cvt_pk_bf16_f32 v219, v74, v75
	v_cvt_pk_bf16_f32 v240, v76, v77
	v_mfma_f32_16x16x32_bf16 v[56:59], v[234:237], v[242:245], v[56:59]
	v_cvt_pk_bf16_f32 v241, v78, v79
	ds_read_b128 v[234:237], v209 offset:22528
	s_setprio 0
	s_waitcnt lgkmcnt(4)
	v_mfma_f32_16x16x32_bf16 v[64:67], v[160:163], v[96:99], 0
	v_exp_f32_e32 v88, v88
	v_mfma_f32_16x16x32_bf16 v[68:71], v[160:163], v[112:115], 0
	v_exp_f32_e32 v92, v92
	ds_read_b128 v[160:163], v201 offset:36864
	s_add_u32 s8, s16, 0x3bc00280
	s_addc_u32 s9, s17, 0
	s_add_u32 s6, s15, 0x23a60000
	s_addc_u32 s7, s14, 0
	v_mfma_f32_16x16x32_bf16 v[0:3], v[164:167], v[216:219], v[0:3]
	v_cvt_pk_bf16_f32 v242, v80, v81
	v_mfma_f32_16x16x32_bf16 v[4:7], v[164:167], v[238:241], v[4:7]
	v_exp_f32_e32 v89, v89
	ds_read_b128 v[164:167], v209 offset:24576
	s_waitcnt vmcnt(4)
	ds_write_b128 v225, v[136:139] offset:0
	v_mfma_f32_16x16x32_bf16 v[68:71], v[168:171], v[116:119], v[68:71]
	v_exp_f32_e32 v93, v93
	v_mfma_f32_16x16x32_bf16 v[64:67], v[168:171], v[100:103], v[64:67]
	v_cvt_pk_bf16_f32 v243, v82, v83
	ds_read_b128 v[168:171], v202 offset:36864
	ds_write_b128 v226, v[140:143] offset:0
	v_mfma_f32_16x16x32_bf16 v[12:15], v[172:175], v[238:241], v[12:15]
	v_exp_f32_e32 v90, v90
	v_mfma_f32_16x16x32_bf16 v[8:11], v[172:175], v[216:219], v[8:11]
	v_exp_f32_e32 v94, v94
	ds_read_b128 v[172:175], v209 offset:26624
	ds_write_b64 v227, v[148:149] offset:49152
	s_waitcnt lgkmcnt(7)
	v_mfma_f32_16x16x32_bf16 v[64:67], v[176:179], v[104:107], v[64:67]
	v_cvt_pk_bf16_f32 v204, v84, v85
	v_mfma_f32_16x16x32_bf16 v[68:71], v[176:179], v[120:123], v[68:71]
	v_exp_f32_e32 v91, v91
	ds_read_b128 v[176:179], v203 offset:36864
	ds_write_b64 v228, v[150:151] offset:49152
	v_mfma_f32_16x16x32_bf16 v[16:19], v[180:183], v[216:219], v[16:19]
	v_exp_f32_e32 v95, v95
	v_mfma_f32_16x16x32_bf16 v[20:23], v[180:183], v[238:241], v[20:23]
	v_cvt_pk_bf16_f32 v205, v86, v87
	v_add_f32_e32 v220, v220, v88
	ds_read_b128 v[180:183], v209 offset:28672
	ds_write_b64 v229, v[144:145] offset:49152
	v_mfma_f32_16x16x32_bf16 v[68:71], v[230:233], v[124:127], v[68:71]
	v_add_f32_e32 v221, v221, v92
	v_add_f32_e32 v220, v220, v89
	v_mfma_f32_16x16x32_bf16 v[64:67], v[230:233], v[108:111], v[64:67]
	v_add_f32_e32 v221, v221, v93
	v_cvt_pk_bf16_f32 v244, v88, v89
	ds_read_b128 v[230:233], v246 offset:36864
	ds_write_b64 v184, v[146:147] offset:49152
	v_mfma_f32_16x16x32_bf16 v[28:31], v[234:237], v[238:241], v[28:31]
	v_cvt_pk_bf16_f32 v245, v90, v91
	v_cvt_pk_bf16_f32 v206, v92, v93
	v_mfma_f32_16x16x32_bf16 v[24:27], v[234:237], v[216:219], v[24:27]
	v_cvt_pk_bf16_f32 v207, v94, v95
	ds_read_b128 v[234:237], v209 offset:30720
	global_load_dwordx4 v[148:151], v198, s[8:9]
	s_waitcnt lgkmcnt(8)
	v_mfma_f32_16x16x32_bf16 v[72:75], v[160:163], v[96:99], 0
	v_add_f32_e32 v220, v220, v90
	v_add_f32_e32 v221, v221, v94
	v_mfma_f32_16x16x32_bf16 v[76:79], v[160:163], v[112:115], 0
	v_add_f32_e32 v220, v220, v91
	v_add_f32_e32 v221, v221, v95
	ds_read_b128 v[160:163], v201 offset:40960
	global_load_dwordx4 v[144:147], v199, s[8:9]
	v_mfma_f32_16x16x32_bf16 v[32:35], v[164:167], v[216:219], v[32:35]
	v_add_f32_e32 v194, v194, v220
	v_add_f32_e32 v195, v195, v221
	v_mfma_f32_16x16x32_bf16 v[36:39], v[164:167], v[238:241], v[36:39]
	v_exp_f32_e32 v64, v64
	ds_read_b128 v[164:167], v210 offset:16384
	global_load_dwordx4 v[136:139], v196, s[6:7]
	v_mfma_f32_16x16x32_bf16 v[76:79], v[168:171], v[116:119], v[76:79]
	v_exp_f32_e32 v68, v68
	v_mfma_f32_16x16x32_bf16 v[72:75], v[168:171], v[100:103], v[72:75]
	v_exp_f32_e32 v65, v65
	ds_read_b128 v[168:171], v202 offset:40960
	global_load_dwordx4 v[140:143], v197, s[6:7]
	v_mfma_f32_16x16x32_bf16 v[44:47], v[172:175], v[238:241], v[44:47]
	v_exp_f32_e32 v69, v69
	v_mfma_f32_16x16x32_bf16 v[40:43], v[172:175], v[216:219], v[40:43]
	v_exp_f32_e32 v66, v66
	ds_read_b128 v[172:175], v210 offset:18432
	s_waitcnt lgkmcnt(4)
	v_mfma_f32_16x16x32_bf16 v[72:75], v[176:179], v[104:107], v[72:75]
	v_exp_f32_e32 v70, v70
	v_mfma_f32_16x16x32_bf16 v[76:79], v[176:179], v[120:123], v[76:79]
	v_exp_f32_e32 v67, v67
	ds_read_b128 v[176:179], v203 offset:40960
	v_mfma_f32_16x16x32_bf16 v[48:51], v[180:183], v[216:219], v[48:51]
	v_exp_f32_e32 v71, v71
	v_mfma_f32_16x16x32_bf16 v[52:55], v[180:183], v[238:241], v[52:55]
	v_add_f32_e32 v220, v64, v65
	ds_read_b128 v[180:183], v210 offset:20480
	v_mfma_f32_16x16x32_bf16 v[76:79], v[230:233], v[124:127], v[76:79]
	v_add_f32_e32 v221, v68, v69
	v_mfma_f32_16x16x32_bf16 v[72:75], v[230:233], v[108:111], v[72:75]
	v_add_f32_e32 v220, v220, v66
	ds_read_b128 v[230:233], v246 offset:40960
	v_mfma_f32_16x16x32_bf16 v[60:63], v[234:237], v[238:241], v[60:63]
	v_add_f32_e32 v221, v221, v70
	v_add_f32_e32 v220, v220, v67
	v_mfma_f32_16x16x32_bf16 v[56:59], v[234:237], v[216:219], v[56:59]
	v_add_f32_e32 v221, v221, v71
	ds_read_b128 v[234:237], v210 offset:22528
	s_waitcnt lgkmcnt(4)
	v_mfma_f32_16x16x32_bf16 v[80:83], v[160:163], v[96:99], 0
	v_exp_f32_e32 v72, v72
	v_mfma_f32_16x16x32_bf16 v[84:87], v[160:163], v[112:115], 0
	v_exp_f32_e32 v76, v76
	ds_read_b128 v[160:163], v201 offset:45056
	v_mfma_f32_16x16x32_bf16 v[0:3], v[164:167], v[242:245], v[0:3]
	v_exp_f32_e32 v73, v73
	v_mfma_f32_16x16x32_bf16 v[4:7], v[164:167], v[204:207], v[4:7]
	v_exp_f32_e32 v77, v77
	ds_read_b128 v[164:167], v210 offset:24576
	v_mfma_f32_16x16x32_bf16 v[84:87], v[168:171], v[116:119], v[84:87]
	v_exp_f32_e32 v74, v74
	v_mfma_f32_16x16x32_bf16 v[80:83], v[168:171], v[100:103], v[80:83]
	v_exp_f32_e32 v78, v78
	ds_read_b128 v[168:171], v202 offset:45056
	v_mfma_f32_16x16x32_bf16 v[12:15], v[172:175], v[204:207], v[12:15]
	v_exp_f32_e32 v75, v75
	v_mfma_f32_16x16x32_bf16 v[8:11], v[172:175], v[242:245], v[8:11]
	v_exp_f32_e32 v79, v79
	ds_read_b128 v[172:175], v210 offset:26624
	s_waitcnt lgkmcnt(4)
	v_mfma_f32_16x16x32_bf16 v[80:83], v[176:179], v[104:107], v[80:83]
	v_add_f32_e32 v220, v220, v72
	v_add_f32_e32 v221, v221, v76
	v_mfma_f32_16x16x32_bf16 v[84:87], v[176:179], v[120:123], v[84:87]
	v_add_f32_e32 v220, v220, v73
	ds_read_b128 v[176:179], v203 offset:45056
	v_mfma_f32_16x16x32_bf16 v[16:19], v[180:183], v[242:245], v[16:19]
	v_add_f32_e32 v221, v221, v77
	v_add_f32_e32 v220, v220, v74
	v_mfma_f32_16x16x32_bf16 v[20:23], v[180:183], v[204:207], v[20:23]
	v_add_f32_e32 v221, v221, v78
	ds_read_b128 v[180:183], v210 offset:28672
	v_mfma_f32_16x16x32_bf16 v[84:87], v[230:233], v[124:127], v[84:87]
	v_add_f32_e32 v220, v220, v75
	v_add_f32_e32 v221, v221, v79
	v_mfma_f32_16x16x32_bf16 v[80:83], v[230:233], v[108:111], v[80:83]
	v_cvt_pk_bf16_f32 v216, v64, v65
	ds_read_b128 v[230:233], v246 offset:45056
	v_mfma_f32_16x16x32_bf16 v[28:31], v[234:237], v[204:207], v[28:31]
	v_cvt_pk_bf16_f32 v217, v66, v67
	v_cvt_pk_bf16_f32 v238, v68, v69
	v_mfma_f32_16x16x32_bf16 v[24:27], v[234:237], v[242:245], v[24:27]
	v_cvt_pk_bf16_f32 v239, v70, v71
	ds_read_b128 v[234:237], v210 offset:30720
	s_waitcnt lgkmcnt(4)
	v_mfma_f32_16x16x32_bf16 v[88:91], v[160:163], v[96:99], 0
	v_exp_f32_e32 v80, v80
	v_mfma_f32_16x16x32_bf16 v[92:95], v[160:163], v[112:115], 0
	v_exp_f32_e32 v84, v84
	v_mfma_f32_16x16x32_bf16 v[32:35], v[164:167], v[242:245], v[32:35]
	v_exp_f32_e32 v81, v81
	v_mfma_f32_16x16x32_bf16 v[36:39], v[164:167], v[204:207], v[36:39]
	v_exp_f32_e32 v85, v85
	v_mfma_f32_16x16x32_bf16 v[92:95], v[168:171], v[116:119], v[92:95]
	v_exp_f32_e32 v82, v82
	v_mfma_f32_16x16x32_bf16 v[88:91], v[168:171], v[100:103], v[88:91]
	v_exp_f32_e32 v86, v86
	v_mfma_f32_16x16x32_bf16 v[44:47], v[172:175], v[204:207], v[44:47]
	v_exp_f32_e32 v83, v83
	v_mfma_f32_16x16x32_bf16 v[40:43], v[172:175], v[242:245], v[40:43]
	v_exp_f32_e32 v87, v87
	s_waitcnt lgkmcnt(3)
	v_mfma_f32_16x16x32_bf16 v[88:91], v[176:179], v[104:107], v[88:91]
	v_add_f32_e32 v220, v220, v80
	v_add_f32_e32 v221, v221, v84
	v_mfma_f32_16x16x32_bf16 v[92:95], v[176:179], v[120:123], v[92:95]
	v_add_f32_e32 v220, v220, v81
	s_waitcnt lgkmcnt(0)
	s_barrier
	ds_read_b128 v[160:163], v201 offset:49152
	ds_read_b128 v[164:167], v209 offset:32768
	ds_read_b128 v[168:171], v202 offset:49152
	ds_read_b128 v[172:175], v209 offset:34816
	ds_read_b128 v[176:179], v203 offset:49152
	v_mfma_f32_16x16x32_bf16 v[48:51], v[180:183], v[242:245], v[48:51]
	v_add_f32_e32 v221, v221, v85
	v_add_f32_e32 v220, v220, v82
	v_mfma_f32_16x16x32_bf16 v[52:55], v[180:183], v[204:207], v[52:55]
	v_add_f32_e32 v221, v221, v86
	ds_read_b128 v[180:183], v209 offset:36864
	v_mfma_f32_16x16x32_bf16 v[92:95], v[230:233], v[124:127], v[92:95]
	v_add_f32_e32 v220, v220, v83
	v_add_f32_e32 v221, v221, v87
	v_mfma_f32_16x16x32_bf16 v[88:91], v[230:233], v[108:111], v[88:91]
	v_cvt_pk_bf16_f32 v218, v72, v73
	ds_read_b128 v[230:233], v246 offset:49152
	v_mfma_f32_16x16x32_bf16 v[60:63], v[234:237], v[204:207], v[60:63]
	v_cvt_pk_bf16_f32 v219, v74, v75
	v_cvt_pk_bf16_f32 v240, v76, v77
	v_mfma_f32_16x16x32_bf16 v[56:59], v[234:237], v[242:245], v[56:59]
	v_cvt_pk_bf16_f32 v241, v78, v79
	ds_read_b128 v[234:237], v209 offset:38912
	s_cmp_eq_u32 s100, 0
	s_cbranch_scc1 .Lattn_pa2
	s_setprio 1
.Lattn_pa2:
	s_waitcnt lgkmcnt(4)
	v_mfma_f32_16x16x32_bf16 v[64:67], v[160:163], v[96:99], 0
	v_exp_f32_e32 v88, v88
	v_mfma_f32_16x16x32_bf16 v[68:71], v[160:163], v[112:115], 0
	v_exp_f32_e32 v92, v92
	ds_read_b128 v[160:163], v201 offset:53248
	s_add_u32 s8, s16, 0x3bc00300
	s_addc_u32 s9, s17, 0
	s_add_u32 s6, s15, 0x23a70000
	s_addc_u32 s7, s14, 0
	v_mfma_f32_16x16x32_bf16 v[0:3], v[164:167], v[216:219], v[0:3]
	v_cvt_pk_bf16_f32 v242, v80, v81
	v_mfma_f32_16x16x32_bf16 v[4:7], v[164:167], v[238:241], v[4:7]
	v_exp_f32_e32 v89, v89
	ds_read_b128 v[164:167], v209 offset:40960
	s_waitcnt vmcnt(4)
	ds_write_b128 v225, v[152:155] offset:16384
	v_mfma_f32_16x16x32_bf16 v[68:71], v[168:171], v[116:119], v[68:71]
	v_exp_f32_e32 v93, v93
	v_mfma_f32_16x16x32_bf16 v[64:67], v[168:171], v[100:103], v[64:67]
	v_cvt_pk_bf16_f32 v243, v82, v83
	ds_read_b128 v[168:171], v202 offset:53248
	ds_write_b128 v226, v[156:159] offset:16384
	v_mfma_f32_16x16x32_bf16 v[12:15], v[172:175], v[238:241], v[12:15]
	v_exp_f32_e32 v90, v90
	v_mfma_f32_16x16x32_bf16 v[8:11], v[172:175], v[216:219], v[8:11]
	v_exp_f32_e32 v94, v94
	ds_read_b128 v[172:175], v209 offset:43008
	ds_write_b64 v227, v[132:133] offset:0
	s_waitcnt lgkmcnt(7)
	v_mfma_f32_16x16x32_bf16 v[64:67], v[176:179], v[104:107], v[64:67]
	v_cvt_pk_bf16_f32 v204, v84, v85
	v_mfma_f32_16x16x32_bf16 v[68:71], v[176:179], v[120:123], v[68:71]
	v_exp_f32_e32 v91, v91
	ds_read_b128 v[176:179], v203 offset:53248
	ds_write_b64 v228, v[134:135] offset:0
	v_mfma_f32_16x16x32_bf16 v[16:19], v[180:183], v[216:219], v[16:19]
	v_exp_f32_e32 v95, v95
	v_mfma_f32_16x16x32_bf16 v[20:23], v[180:183], v[238:241], v[20:23]
	v_cvt_pk_bf16_f32 v205, v86, v87
	v_add_f32_e32 v220, v220, v88
	ds_read_b128 v[180:183], v209 offset:45056
	ds_write_b64 v229, v[128:129] offset:0
	v_mfma_f32_16x16x32_bf16 v[68:71], v[230:233], v[124:127], v[68:71]
	v_add_f32_e32 v221, v221, v92
	v_add_f32_e32 v220, v220, v89
	v_mfma_f32_16x16x32_bf16 v[64:67], v[230:233], v[108:111], v[64:67]
	v_add_f32_e32 v221, v221, v93
	v_cvt_pk_bf16_f32 v244, v88, v89
	ds_read_b128 v[230:233], v246 offset:53248
	ds_write_b64 v184, v[130:131] offset:0
	v_mfma_f32_16x16x32_bf16 v[28:31], v[234:237], v[238:241], v[28:31]
	v_cvt_pk_bf16_f32 v245, v90, v91
	v_cvt_pk_bf16_f32 v206, v92, v93
	v_mfma_f32_16x16x32_bf16 v[24:27], v[234:237], v[216:219], v[24:27]
	v_cvt_pk_bf16_f32 v207, v94, v95
	ds_read_b128 v[234:237], v209 offset:47104
	global_load_dwordx4 v[132:135], v198, s[8:9]
	s_waitcnt lgkmcnt(8)
	v_mfma_f32_16x16x32_bf16 v[72:75], v[160:163], v[96:99], 0
	v_add_f32_e32 v220, v220, v90
	v_add_f32_e32 v221, v221, v94
	v_mfma_f32_16x16x32_bf16 v[76:79], v[160:163], v[112:115], 0
	v_add_f32_e32 v220, v220, v91
	v_add_f32_e32 v221, v221, v95
	ds_read_b128 v[160:163], v201 offset:57344
	global_load_dwordx4 v[128:131], v199, s[8:9]
	v_mfma_f32_16x16x32_bf16 v[32:35], v[164:167], v[216:219], v[32:35]
	v_add_f32_e32 v194, v194, v220
	v_add_f32_e32 v195, v195, v221
	v_mfma_f32_16x16x32_bf16 v[36:39], v[164:167], v[238:241], v[36:39]
	v_exp_f32_e32 v64, v64
	ds_read_b128 v[164:167], v210 offset:32768
	global_load_dwordx4 v[152:155], v196, s[6:7]
	v_mfma_f32_16x16x32_bf16 v[76:79], v[168:171], v[116:119], v[76:79]
	v_exp_f32_e32 v68, v68
	v_mfma_f32_16x16x32_bf16 v[72:75], v[168:171], v[100:103], v[72:75]
	v_exp_f32_e32 v65, v65
	ds_read_b128 v[168:171], v202 offset:57344
	global_load_dwordx4 v[156:159], v197, s[6:7]
	v_mfma_f32_16x16x32_bf16 v[44:47], v[172:175], v[238:241], v[44:47]
	v_exp_f32_e32 v69, v69
	v_mfma_f32_16x16x32_bf16 v[40:43], v[172:175], v[216:219], v[40:43]
	v_exp_f32_e32 v66, v66
	ds_read_b128 v[172:175], v210 offset:34816
	s_waitcnt lgkmcnt(4)
	v_mfma_f32_16x16x32_bf16 v[72:75], v[176:179], v[104:107], v[72:75]
	v_exp_f32_e32 v70, v70
	v_mfma_f32_16x16x32_bf16 v[76:79], v[176:179], v[120:123], v[76:79]
	v_exp_f32_e32 v67, v67
	ds_read_b128 v[176:179], v203 offset:57344
	v_mfma_f32_16x16x32_bf16 v[48:51], v[180:183], v[216:219], v[48:51]
	v_exp_f32_e32 v71, v71
	v_mfma_f32_16x16x32_bf16 v[52:55], v[180:183], v[238:241], v[52:55]
	v_add_f32_e32 v220, v64, v65
	ds_read_b128 v[180:183], v210 offset:36864
	v_mfma_f32_16x16x32_bf16 v[76:79], v[230:233], v[124:127], v[76:79]
	v_add_f32_e32 v221, v68, v69
	v_mfma_f32_16x16x32_bf16 v[72:75], v[230:233], v[108:111], v[72:75]
	v_add_f32_e32 v220, v220, v66
	ds_read_b128 v[230:233], v246 offset:57344
	v_mfma_f32_16x16x32_bf16 v[60:63], v[234:237], v[238:241], v[60:63]
	v_add_f32_e32 v221, v221, v70
	v_add_f32_e32 v220, v220, v67
	v_mfma_f32_16x16x32_bf16 v[56:59], v[234:237], v[216:219], v[56:59]
	v_add_f32_e32 v221, v221, v71
	ds_read_b128 v[234:237], v210 offset:38912
	s_waitcnt lgkmcnt(4)
	v_mfma_f32_16x16x32_bf16 v[80:83], v[160:163], v[96:99], 0
	v_exp_f32_e32 v72, v72
	v_mfma_f32_16x16x32_bf16 v[84:87], v[160:163], v[112:115], 0
	v_exp_f32_e32 v76, v76
	ds_read_b128 v[160:163], v201 offset:61440
	v_mfma_f32_16x16x32_bf16 v[0:3], v[164:167], v[242:245], v[0:3]
	v_exp_f32_e32 v73, v73
	v_mfma_f32_16x16x32_bf16 v[4:7], v[164:167], v[204:207], v[4:7]
	v_exp_f32_e32 v77, v77
	ds_read_b128 v[164:167], v210 offset:40960
	v_mfma_f32_16x16x32_bf16 v[84:87], v[168:171], v[116:119], v[84:87]
	v_exp_f32_e32 v74, v74
	v_mfma_f32_16x16x32_bf16 v[80:83], v[168:171], v[100:103], v[80:83]
	v_exp_f32_e32 v78, v78
	ds_read_b128 v[168:171], v202 offset:61440
	v_mfma_f32_16x16x32_bf16 v[12:15], v[172:175], v[204:207], v[12:15]
	v_exp_f32_e32 v75, v75
	v_mfma_f32_16x16x32_bf16 v[8:11], v[172:175], v[242:245], v[8:11]
	v_exp_f32_e32 v79, v79
	ds_read_b128 v[172:175], v210 offset:43008
	s_waitcnt lgkmcnt(4)
	v_mfma_f32_16x16x32_bf16 v[80:83], v[176:179], v[104:107], v[80:83]
	v_add_f32_e32 v220, v220, v72
	v_add_f32_e32 v221, v221, v76
	v_mfma_f32_16x16x32_bf16 v[84:87], v[176:179], v[120:123], v[84:87]
	v_add_f32_e32 v220, v220, v73
	ds_read_b128 v[176:179], v203 offset:61440
	v_mfma_f32_16x16x32_bf16 v[16:19], v[180:183], v[242:245], v[16:19]
	v_add_f32_e32 v221, v221, v77
	v_add_f32_e32 v220, v220, v74
	v_mfma_f32_16x16x32_bf16 v[20:23], v[180:183], v[204:207], v[20:23]
	v_add_f32_e32 v221, v221, v78
	ds_read_b128 v[180:183], v210 offset:45056
	v_mfma_f32_16x16x32_bf16 v[84:87], v[230:233], v[124:127], v[84:87]
	v_add_f32_e32 v220, v220, v75
	v_add_f32_e32 v221, v221, v79
	v_mfma_f32_16x16x32_bf16 v[80:83], v[230:233], v[108:111], v[80:83]
	v_cvt_pk_bf16_f32 v216, v64, v65
	ds_read_b128 v[230:233], v246 offset:61440
	v_mfma_f32_16x16x32_bf16 v[28:31], v[234:237], v[204:207], v[28:31]
	v_cvt_pk_bf16_f32 v217, v66, v67
	v_cvt_pk_bf16_f32 v238, v68, v69
	v_mfma_f32_16x16x32_bf16 v[24:27], v[234:237], v[242:245], v[24:27]
	v_cvt_pk_bf16_f32 v239, v70, v71
	ds_read_b128 v[234:237], v210 offset:47104
	s_waitcnt lgkmcnt(4)
	v_mfma_f32_16x16x32_bf16 v[88:91], v[160:163], v[96:99], 0
	v_exp_f32_e32 v80, v80
	v_mfma_f32_16x16x32_bf16 v[92:95], v[160:163], v[112:115], 0
	v_exp_f32_e32 v84, v84
	ds_read_b128 v[160:163], v201 offset:0
	v_mfma_f32_16x16x32_bf16 v[32:35], v[164:167], v[242:245], v[32:35]
	v_exp_f32_e32 v81, v81
	v_mfma_f32_16x16x32_bf16 v[36:39], v[164:167], v[204:207], v[36:39]
	v_exp_f32_e32 v85, v85
	ds_read_b128 v[164:167], v209 offset:49152
	v_mfma_f32_16x16x32_bf16 v[92:95], v[168:171], v[116:119], v[92:95]
	v_exp_f32_e32 v82, v82
	v_mfma_f32_16x16x32_bf16 v[88:91], v[168:171], v[100:103], v[88:91]
	v_exp_f32_e32 v86, v86
	ds_read_b128 v[168:171], v202 offset:0
	v_mfma_f32_16x16x32_bf16 v[44:47], v[172:175], v[204:207], v[44:47]
	v_exp_f32_e32 v83, v83
	v_mfma_f32_16x16x32_bf16 v[40:43], v[172:175], v[242:245], v[40:43]
	v_exp_f32_e32 v87, v87
	ds_read_b128 v[172:175], v209 offset:51200
	s_waitcnt lgkmcnt(4)
	v_mfma_f32_16x16x32_bf16 v[88:91], v[176:179], v[104:107], v[88:91]
	v_add_f32_e32 v220, v220, v80
	v_add_f32_e32 v221, v221, v84
	v_mfma_f32_16x16x32_bf16 v[92:95], v[176:179], v[120:123], v[92:95]
	v_add_f32_e32 v220, v220, v81
	ds_read_b128 v[176:179], v203 offset:0
	v_mfma_f32_16x16x32_bf16 v[48:51], v[180:183], v[242:245], v[48:51]
	v_add_f32_e32 v221, v221, v85
	v_add_f32_e32 v220, v220, v82
	v_mfma_f32_16x16x32_bf16 v[52:55], v[180:183], v[204:207], v[52:55]
	v_add_f32_e32 v221, v221, v86
	ds_read_b128 v[180:183], v209 offset:53248
	v_mfma_f32_16x16x32_bf16 v[92:95], v[230:233], v[124:127], v[92:95]
	v_add_f32_e32 v220, v220, v83
	v_add_f32_e32 v221, v221, v87
	v_mfma_f32_16x16x32_bf16 v[88:91], v[230:233], v[108:111], v[88:91]
	v_cvt_pk_bf16_f32 v218, v72, v73
	ds_read_b128 v[230:233], v246 offset:0
	v_mfma_f32_16x16x32_bf16 v[60:63], v[234:237], v[204:207], v[60:63]
	v_cvt_pk_bf16_f32 v219, v74, v75
	v_cvt_pk_bf16_f32 v240, v76, v77
	v_mfma_f32_16x16x32_bf16 v[56:59], v[234:237], v[242:245], v[56:59]
	v_cvt_pk_bf16_f32 v241, v78, v79
	ds_read_b128 v[234:237], v209 offset:55296
	s_setprio 0
	s_waitcnt lgkmcnt(4)
	v_mfma_f32_16x16x32_bf16 v[64:67], v[160:163], v[96:99], 0
	v_exp_f32_e32 v88, v88
	v_mfma_f32_16x16x32_bf16 v[68:71], v[160:163], v[112:115], 0
	v_exp_f32_e32 v92, v92
	ds_read_b128 v[160:163], v201 offset:4096
	s_add_u32 s8, s16, 0x3bc00380
	s_addc_u32 s9, s17, 0
	s_add_u32 s6, s15, 0x23a80000
	s_addc_u32 s7, s14, 0
	v_mfma_f32_16x16x32_bf16 v[0:3], v[164:167], v[216:219], v[0:3]
	v_cvt_pk_bf16_f32 v242, v80, v81
	v_mfma_f32_16x16x32_bf16 v[4:7], v[164:167], v[238:241], v[4:7]
	v_exp_f32_e32 v89, v89
	ds_read_b128 v[164:167], v209 offset:57344
	s_waitcnt vmcnt(4)
	ds_write_b128 v225, v[136:139] offset:32768
	v_mfma_f32_16x16x32_bf16 v[68:71], v[168:171], v[116:119], v[68:71]
	v_exp_f32_e32 v93, v93
	v_mfma_f32_16x16x32_bf16 v[64:67], v[168:171], v[100:103], v[64:67]
	v_cvt_pk_bf16_f32 v243, v82, v83
	ds_read_b128 v[168:171], v202 offset:4096
	ds_write_b128 v226, v[140:143] offset:32768
	v_mfma_f32_16x16x32_bf16 v[12:15], v[172:175], v[238:241], v[12:15]
	v_exp_f32_e32 v90, v90
	v_mfma_f32_16x16x32_bf16 v[8:11], v[172:175], v[216:219], v[8:11]
	v_exp_f32_e32 v94, v94
	ds_read_b128 v[172:175], v209 offset:59392
	ds_write_b64 v227, v[148:149] offset:16384
	s_waitcnt lgkmcnt(7)
	v_mfma_f32_16x16x32_bf16 v[64:67], v[176:179], v[104:107], v[64:67]
	v_cvt_pk_bf16_f32 v204, v84, v85
	v_mfma_f32_16x16x32_bf16 v[68:71], v[176:179], v[120:123], v[68:71]
	v_exp_f32_e32 v91, v91
	ds_read_b128 v[176:179], v203 offset:4096
	ds_write_b64 v228, v[150:151] offset:16384
	v_mfma_f32_16x16x32_bf16 v[16:19], v[180:183], v[216:219], v[16:19]
	v_exp_f32_e32 v95, v95
	v_mfma_f32_16x16x32_bf16 v[20:23], v[180:183], v[238:241], v[20:23]
	v_cvt_pk_bf16_f32 v205, v86, v87
	v_add_f32_e32 v220, v220, v88
	ds_read_b128 v[180:183], v209 offset:61440
	ds_write_b64 v229, v[144:145] offset:16384
	v_mfma_f32_16x16x32_bf16 v[68:71], v[230:233], v[124:127], v[68:71]
	v_add_f32_e32 v221, v221, v92
	v_add_f32_e32 v220, v220, v89
	v_mfma_f32_16x16x32_bf16 v[64:67], v[230:233], v[108:111], v[64:67]
	v_add_f32_e32 v221, v221, v93
	v_cvt_pk_bf16_f32 v244, v88, v89
	ds_read_b128 v[230:233], v246 offset:4096
	ds_write_b64 v184, v[146:147] offset:16384
	v_mfma_f32_16x16x32_bf16 v[28:31], v[234:237], v[238:241], v[28:31]
	v_cvt_pk_bf16_f32 v245, v90, v91
	v_cvt_pk_bf16_f32 v206, v92, v93
	v_mfma_f32_16x16x32_bf16 v[24:27], v[234:237], v[216:219], v[24:27]
	v_cvt_pk_bf16_f32 v207, v94, v95
	ds_read_b128 v[234:237], v209 offset:63488
	global_load_dwordx4 v[148:151], v198, s[8:9]
	s_waitcnt lgkmcnt(8)
	v_mfma_f32_16x16x32_bf16 v[72:75], v[160:163], v[96:99], 0
	v_add_f32_e32 v220, v220, v90
	v_add_f32_e32 v221, v221, v94
	v_mfma_f32_16x16x32_bf16 v[76:79], v[160:163], v[112:115], 0
	v_add_f32_e32 v220, v220, v91
	v_add_f32_e32 v221, v221, v95
	ds_read_b128 v[160:163], v201 offset:8192
	global_load_dwordx4 v[144:147], v199, s[8:9]
	v_mfma_f32_16x16x32_bf16 v[32:35], v[164:167], v[216:219], v[32:35]
	v_add_f32_e32 v194, v194, v220
	v_add_f32_e32 v195, v195, v221
	v_mfma_f32_16x16x32_bf16 v[36:39], v[164:167], v[238:241], v[36:39]
	v_exp_f32_e32 v64, v64
	ds_read_b128 v[164:167], v210 offset:49152
	global_load_dwordx4 v[136:139], v196, s[6:7]
	v_mfma_f32_16x16x32_bf16 v[76:79], v[168:171], v[116:119], v[76:79]
	v_exp_f32_e32 v68, v68
	v_mfma_f32_16x16x32_bf16 v[72:75], v[168:171], v[100:103], v[72:75]
	v_exp_f32_e32 v65, v65
	ds_read_b128 v[168:171], v202 offset:8192
	global_load_dwordx4 v[140:143], v197, s[6:7]
	v_mfma_f32_16x16x32_bf16 v[44:47], v[172:175], v[238:241], v[44:47]
	v_exp_f32_e32 v69, v69
	v_mfma_f32_16x16x32_bf16 v[40:43], v[172:175], v[216:219], v[40:43]
	v_exp_f32_e32 v66, v66
	ds_read_b128 v[172:175], v210 offset:51200
	s_waitcnt lgkmcnt(4)
	v_mfma_f32_16x16x32_bf16 v[72:75], v[176:179], v[104:107], v[72:75]
	v_exp_f32_e32 v70, v70
	v_mfma_f32_16x16x32_bf16 v[76:79], v[176:179], v[120:123], v[76:79]
	v_exp_f32_e32 v67, v67
	ds_read_b128 v[176:179], v203 offset:8192
	v_mfma_f32_16x16x32_bf16 v[48:51], v[180:183], v[216:219], v[48:51]
	v_exp_f32_e32 v71, v71
	v_mfma_f32_16x16x32_bf16 v[52:55], v[180:183], v[238:241], v[52:55]
	v_add_f32_e32 v220, v64, v65
	ds_read_b128 v[180:183], v210 offset:53248
	v_mfma_f32_16x16x32_bf16 v[76:79], v[230:233], v[124:127], v[76:79]
	v_add_f32_e32 v221, v68, v69
	v_mfma_f32_16x16x32_bf16 v[72:75], v[230:233], v[108:111], v[72:75]
	v_add_f32_e32 v220, v220, v66
	ds_read_b128 v[230:233], v246 offset:8192
	v_mfma_f32_16x16x32_bf16 v[60:63], v[234:237], v[238:241], v[60:63]
	v_add_f32_e32 v221, v221, v70
	v_add_f32_e32 v220, v220, v67
	v_mfma_f32_16x16x32_bf16 v[56:59], v[234:237], v[216:219], v[56:59]
	v_add_f32_e32 v221, v221, v71
	ds_read_b128 v[234:237], v210 offset:55296
	s_waitcnt lgkmcnt(4)
	v_mfma_f32_16x16x32_bf16 v[80:83], v[160:163], v[96:99], 0
	v_exp_f32_e32 v72, v72
	v_mfma_f32_16x16x32_bf16 v[84:87], v[160:163], v[112:115], 0
	v_exp_f32_e32 v76, v76
	ds_read_b128 v[160:163], v201 offset:12288
	v_mfma_f32_16x16x32_bf16 v[0:3], v[164:167], v[242:245], v[0:3]
	v_exp_f32_e32 v73, v73
	v_mfma_f32_16x16x32_bf16 v[4:7], v[164:167], v[204:207], v[4:7]
	v_exp_f32_e32 v77, v77
	ds_read_b128 v[164:167], v210 offset:57344
	v_mfma_f32_16x16x32_bf16 v[84:87], v[168:171], v[116:119], v[84:87]
	v_exp_f32_e32 v74, v74
	v_mfma_f32_16x16x32_bf16 v[80:83], v[168:171], v[100:103], v[80:83]
	v_exp_f32_e32 v78, v78
	ds_read_b128 v[168:171], v202 offset:12288
	v_mfma_f32_16x16x32_bf16 v[12:15], v[172:175], v[204:207], v[12:15]
	v_exp_f32_e32 v75, v75
	v_mfma_f32_16x16x32_bf16 v[8:11], v[172:175], v[242:245], v[8:11]
	v_exp_f32_e32 v79, v79
	ds_read_b128 v[172:175], v210 offset:59392
	s_waitcnt lgkmcnt(4)
	v_mfma_f32_16x16x32_bf16 v[80:83], v[176:179], v[104:107], v[80:83]
	v_add_f32_e32 v220, v220, v72
	v_add_f32_e32 v221, v221, v76
	v_mfma_f32_16x16x32_bf16 v[84:87], v[176:179], v[120:123], v[84:87]
	v_add_f32_e32 v220, v220, v73
	ds_read_b128 v[176:179], v203 offset:12288
	s_add_u32 s10, s10, 0x200
	s_addc_u32 s11, s11, 0
	s_add_u32 s12, s12, 0x40000
	s_addc_u32 s13, s13, 0
	s_add_i32 s4, s4, 4
	s_cmpk_lt_u32 s4, 0x104
	s_cselect_b64 s[6:7], -1, 0
	s_and_b64 s[6:7], s[0:1], s[6:7]
	s_and_b64 vcc, exec, s[6:7]
	v_mfma_f32_16x16x32_bf16 v[16:19], v[180:183], v[242:245], v[16:19]
	v_add_f32_e32 v221, v221, v77
	v_add_f32_e32 v220, v220, v74
	v_mfma_f32_16x16x32_bf16 v[20:23], v[180:183], v[204:207], v[20:23]
	v_add_f32_e32 v221, v221, v78
	ds_read_b128 v[180:183], v210 offset:61440
	v_mfma_f32_16x16x32_bf16 v[84:87], v[230:233], v[124:127], v[84:87]
	v_add_f32_e32 v220, v220, v75
	v_add_f32_e32 v221, v221, v79
	v_mfma_f32_16x16x32_bf16 v[80:83], v[230:233], v[108:111], v[80:83]
	v_cvt_pk_bf16_f32 v216, v64, v65
	ds_read_b128 v[230:233], v246 offset:12288
	v_mfma_f32_16x16x32_bf16 v[28:31], v[234:237], v[204:207], v[28:31]
	v_cvt_pk_bf16_f32 v217, v66, v67
	v_cvt_pk_bf16_f32 v238, v68, v69
	v_mfma_f32_16x16x32_bf16 v[24:27], v[234:237], v[242:245], v[24:27]
	v_cvt_pk_bf16_f32 v239, v70, v71
	ds_read_b128 v[234:237], v210 offset:63488
	s_waitcnt lgkmcnt(4)
	v_mfma_f32_16x16x32_bf16 v[88:91], v[160:163], v[96:99], 0
	v_exp_f32_e32 v80, v80
	v_mfma_f32_16x16x32_bf16 v[92:95], v[160:163], v[112:115], 0
	v_exp_f32_e32 v84, v84
	v_mfma_f32_16x16x32_bf16 v[32:35], v[164:167], v[242:245], v[32:35]
	v_exp_f32_e32 v81, v81
	v_mfma_f32_16x16x32_bf16 v[36:39], v[164:167], v[204:207], v[36:39]
	v_exp_f32_e32 v85, v85
	v_mfma_f32_16x16x32_bf16 v[92:95], v[168:171], v[116:119], v[92:95]
	v_exp_f32_e32 v82, v82
	v_mfma_f32_16x16x32_bf16 v[88:91], v[168:171], v[100:103], v[88:91]
	v_exp_f32_e32 v86, v86
	v_mfma_f32_16x16x32_bf16 v[44:47], v[172:175], v[204:207], v[44:47]
	v_exp_f32_e32 v83, v83
	v_mfma_f32_16x16x32_bf16 v[40:43], v[172:175], v[242:245], v[40:43]
	v_exp_f32_e32 v87, v87
	s_waitcnt lgkmcnt(3)
	v_mfma_f32_16x16x32_bf16 v[88:91], v[176:179], v[104:107], v[88:91]
	v_add_f32_e32 v220, v220, v80
	v_add_f32_e32 v221, v221, v84
	v_mfma_f32_16x16x32_bf16 v[92:95], v[176:179], v[120:123], v[92:95]
	v_add_f32_e32 v220, v220, v81
	s_waitcnt lgkmcnt(0)
	s_barrier
	ds_read_b128 v[160:163], v201 offset:16384
	ds_read_b128 v[164:167], v209 offset:0
	ds_read_b128 v[168:171], v202 offset:16384
	ds_read_b128 v[172:175], v209 offset:2048
	ds_read_b128 v[176:179], v203 offset:16384
	v_mfma_f32_16x16x32_bf16 v[48:51], v[180:183], v[242:245], v[48:51]
	v_add_f32_e32 v221, v221, v85
	v_add_f32_e32 v220, v220, v82
	v_mfma_f32_16x16x32_bf16 v[52:55], v[180:183], v[204:207], v[52:55]
	v_add_f32_e32 v221, v221, v86
	ds_read_b128 v[180:183], v209 offset:4096
	v_mfma_f32_16x16x32_bf16 v[92:95], v[230:233], v[124:127], v[92:95]
	v_add_f32_e32 v220, v220, v83
	v_add_f32_e32 v221, v221, v87
	v_mfma_f32_16x16x32_bf16 v[88:91], v[230:233], v[108:111], v[88:91]
	v_cvt_pk_bf16_f32 v218, v72, v73
	ds_read_b128 v[230:233], v246 offset:16384
	v_mfma_f32_16x16x32_bf16 v[60:63], v[234:237], v[204:207], v[60:63]
	v_cvt_pk_bf16_f32 v219, v74, v75
	v_cvt_pk_bf16_f32 v240, v76, v77
	v_mfma_f32_16x16x32_bf16 v[56:59], v[234:237], v[242:245], v[56:59]
	v_cvt_pk_bf16_f32 v241, v78, v79
	ds_read_b128 v[234:237], v209 offset:6144
	s_cbranch_vccnz .LBB0_734
	s_setprio 0
	s_waitcnt vmcnt(0)
	s_nop 7
	s_nop 7
	ds_swizzle_b32 v64, v194 offset:swizzle(SWAP,16)
	s_waitcnt lgkmcnt(0)
	v_add_f32_e32 v194, v194, v64
	v_mov_b32_e32 v65, v194
	s_nop 1
	v_permlane32_swap_b32_e32 v194, v65
	v_add_f32_e32 v194, v194, v65
	s_nop 0
	v_rcp_f32_e32 v66, v194
	ds_swizzle_b32 v64, v195 offset:swizzle(SWAP,16)
	s_waitcnt lgkmcnt(0)
	v_add_f32_e32 v195, v195, v64
	v_mov_b32_e32 v65, v195
	s_nop 1
	v_permlane32_swap_b32_e32 v195, v65
	v_add_f32_e32 v195, v195, v65
	s_nop 0
	v_rcp_f32_e32 v67, v195
	v_readlane_b32 s100, v250, 8
	v_mbcnt_lo_u32_b32 v68, -1, 0
	v_mbcnt_hi_u32_b32 v68, -1, v68
	v_and_b32_e32 v69, 15, v68
	v_lshrrev_b32_e32 v70, 4, v68
	s_lshr_b32 s101, s100, 1
	v_add_u32_e32 v69, s101, v69
	v_lshlrev_b32_e32 v69, 12, v69
	v_and_b32_e32 v71, 1, v70
	v_lshlrev_b32_e32 v71, 5, v71
	v_and_b32_e32 v70, 2, v70
	v_lshl_add_u32 v71, v70, 3, v71
	v_add_u32_e32 v70, v69, v71
	v_add_u32_e32 v71, 0x10000, v70
	v_mul_f32_e32 v0, v0, v66
	v_mul_f32_e32 v1, v1, v66
	v_mul_f32_e32 v2, v2, v66
	v_mul_f32_e32 v3, v3, v66
	v_mul_f32_e32 v8, v8, v66
	v_mul_f32_e32 v9, v9, v66
	v_mul_f32_e32 v10, v10, v66
	v_mul_f32_e32 v11, v11, v66
	v_cvt_pk_bf16_f32 v72, v0, v1
	v_cvt_pk_bf16_f32 v73, v2, v3
	v_cvt_pk_bf16_f32 v74, v8, v9
	v_cvt_pk_bf16_f32 v75, v10, v11
	s_nop 1
	v_permlane16_swap_b32_e32 v72, v74
	v_permlane16_swap_b32_e32 v73, v75
	s_nop 1
	global_store_dwordx4 v70, v[72:75], s[58:59] offset:0
	v_mul_f32_e32 v16, v16, v66
	v_mul_f32_e32 v17, v17, v66
	v_mul_f32_e32 v18, v18, v66
	v_mul_f32_e32 v19, v19, v66
	v_mul_f32_e32 v24, v24, v66
	v_mul_f32_e32 v25, v25, v66
	v_mul_f32_e32 v26, v26, v66
	v_mul_f32_e32 v27, v27, v66
	v_cvt_pk_bf16_f32 v76, v16, v17
	v_cvt_pk_bf16_f32 v77, v18, v19
	v_cvt_pk_bf16_f32 v78, v24, v25
	v_cvt_pk_bf16_f32 v79, v26, v27
	s_nop 1
	v_permlane16_swap_b32_e32 v76, v78
	v_permlane16_swap_b32_e32 v77, v79
	s_nop 1
	global_store_dwordx4 v70, v[76:79], s[58:59] offset:64
	v_mul_f32_e32 v32, v32, v66
	v_mul_f32_e32 v33, v33, v66
	v_mul_f32_e32 v34, v34, v66
	v_mul_f32_e32 v35, v35, v66
	v_mul_f32_e32 v40, v40, v66
	v_mul_f32_e32 v41, v41, v66
	v_mul_f32_e32 v42, v42, v66
	v_mul_f32_e32 v43, v43, v66
	v_cvt_pk_bf16_f32 v80, v32, v33
	v_cvt_pk_bf16_f32 v81, v34, v35
	v_cvt_pk_bf16_f32 v82, v40, v41
	v_cvt_pk_bf16_f32 v83, v42, v43
	s_nop 1
	v_permlane16_swap_b32_e32 v80, v82
	v_permlane16_swap_b32_e32 v81, v83
	s_nop 1
	global_store_dwordx4 v70, v[80:83], s[58:59] offset:128
	v_mul_f32_e32 v48, v48, v66
	v_mul_f32_e32 v49, v49, v66
	v_mul_f32_e32 v50, v50, v66
	v_mul_f32_e32 v51, v51, v66
	v_mul_f32_e32 v56, v56, v66
	v_mul_f32_e32 v57, v57, v66
	v_mul_f32_e32 v58, v58, v66
	v_mul_f32_e32 v59, v59, v66
	v_cvt_pk_bf16_f32 v84, v48, v49
	v_cvt_pk_bf16_f32 v85, v50, v51
	v_cvt_pk_bf16_f32 v86, v56, v57
	v_cvt_pk_bf16_f32 v87, v58, v59
	s_nop 1
	v_permlane16_swap_b32_e32 v84, v86
	v_permlane16_swap_b32_e32 v85, v87
	s_nop 1
	global_store_dwordx4 v70, v[84:87], s[58:59] offset:192
	v_mul_f32_e32 v4, v4, v67
	v_mul_f32_e32 v5, v5, v67
	v_mul_f32_e32 v6, v6, v67
	v_mul_f32_e32 v7, v7, v67
	v_mul_f32_e32 v12, v12, v67
	v_mul_f32_e32 v13, v13, v67
	v_mul_f32_e32 v14, v14, v67
	v_mul_f32_e32 v15, v15, v67
	v_cvt_pk_bf16_f32 v88, v4, v5
	v_cvt_pk_bf16_f32 v89, v6, v7
	v_cvt_pk_bf16_f32 v90, v12, v13
	v_cvt_pk_bf16_f32 v91, v14, v15
	s_nop 1
	v_permlane16_swap_b32_e32 v88, v90
	v_permlane16_swap_b32_e32 v89, v91
	s_nop 1
	global_store_dwordx4 v71, v[88:91], s[58:59] offset:0
	v_mul_f32_e32 v20, v20, v67
	v_mul_f32_e32 v21, v21, v67
	v_mul_f32_e32 v22, v22, v67
	v_mul_f32_e32 v23, v23, v67
	v_mul_f32_e32 v28, v28, v67
	v_mul_f32_e32 v29, v29, v67
	v_mul_f32_e32 v30, v30, v67
	v_mul_f32_e32 v31, v31, v67
	v_cvt_pk_bf16_f32 v92, v20, v21
	v_cvt_pk_bf16_f32 v93, v22, v23
	v_cvt_pk_bf16_f32 v94, v28, v29
	v_cvt_pk_bf16_f32 v95, v30, v31
	s_nop 1
	v_permlane16_swap_b32_e32 v92, v94
	v_permlane16_swap_b32_e32 v93, v95
	s_nop 1
	global_store_dwordx4 v71, v[92:95], s[58:59] offset:64
	v_mul_f32_e32 v36, v36, v67
	v_mul_f32_e32 v37, v37, v67
	v_mul_f32_e32 v38, v38, v67
	v_mul_f32_e32 v39, v39, v67
	v_mul_f32_e32 v44, v44, v67
	v_mul_f32_e32 v45, v45, v67
	v_mul_f32_e32 v46, v46, v67
	v_mul_f32_e32 v47, v47, v67
	v_cvt_pk_bf16_f32 v72, v36, v37
	v_cvt_pk_bf16_f32 v73, v38, v39
	v_cvt_pk_bf16_f32 v74, v44, v45
	v_cvt_pk_bf16_f32 v75, v46, v47
	s_nop 1
	v_permlane16_swap_b32_e32 v72, v74
	v_permlane16_swap_b32_e32 v73, v75
	s_nop 1
	global_store_dwordx4 v71, v[72:75], s[58:59] offset:128
	v_mul_f32_e32 v52, v52, v67
	v_mul_f32_e32 v53, v53, v67
	v_mul_f32_e32 v54, v54, v67
	v_mul_f32_e32 v55, v55, v67
	v_mul_f32_e32 v60, v60, v67
	v_mul_f32_e32 v61, v61, v67
	v_mul_f32_e32 v62, v62, v67
	v_mul_f32_e32 v63, v63, v67
	v_cvt_pk_bf16_f32 v76, v52, v53
	v_cvt_pk_bf16_f32 v77, v54, v55
	v_cvt_pk_bf16_f32 v78, v60, v61
	v_cvt_pk_bf16_f32 v79, v62, v63
	s_nop 1
	v_permlane16_swap_b32_e32 v76, v78
	v_permlane16_swap_b32_e32 v77, v79
	s_nop 1
	global_store_dwordx4 v71, v[76:79], s[58:59] offset:192
	s_barrier
